# v26
# baseline (speedup 1.0000x reference)
.LBB0_15:
	s_or_b64 exec, exec, s[22:23]
	s_waitcnt vmcnt(0)
	v_max3_f32 v19, |v14|, 0, |v15|
	v_max3_f32 v19, v19, |v16|, |v17|
	v_max3_f32 v19, v19, |v10|, |v11|
	v_max3_f32 v19, v19, |v12|, |v13|
	s_nop 1
	v_max_f32_dpp v19, v19, v19 quad_perm:[1,0,3,2] row_mask:0xf bank_mask:0xf bound_ctrl:1
	s_nop 1
	v_max_f32_dpp v19, v19, v19 quad_perm:[2,3,0,1] row_mask:0xf bank_mask:0xf bound_ctrl:1
	s_nop 1
	v_max_f32_dpp v19, v19, v19 row_half_mirror row_mask:0xf bank_mask:0xf bound_ctrl:1
	s_nop 1
	v_max_f32_dpp v19, v19, v19 row_mirror row_mask:0xf bank_mask:0xf bound_ctrl:1
	v_div_scale_f32 v23, s[22:23], v19, v19, s26
	v_rcp_f32_e32 v28, v23
	v_div_scale_f32 v29, vcc, s26, v19, s26
	v_fma_f32 v30, -v23, v28, 1.0
	v_fmac_f32_e32 v28, v30, v28
	v_mul_f32_e32 v30, v29, v28
	v_fma_f32 v31, -v23, v30, v29
	v_fmac_f32_e32 v30, v31, v28
	v_fma_f32 v23, -v23, v30, v29
	v_div_fmas_f32 v23, v23, v28, v30
	v_div_fixup_f32 v23, v23, v19, s26
	v_cmp_lt_f32_e32 vcc, 0, v19
	s_nop 1
	v_cndmask_b32_e32 v23, 0, v23, vcc
	v_mul_f32_e32 v14, v14, v23
	v_mul_f32_e32 v15, v15, v23
	v_mul_f32_e32 v16, v16, v23
	v_mul_f32_e32 v17, v17, v23
	v_mul_f32_e32 v10, v10, v23
	v_mul_f32_e32 v11, v11, v23
	v_mul_f32_e32 v12, v12, v23
	v_mul_f32_e32 v13, v13, v23
	v_rndne_f32_e32 v14, v14
	v_rndne_f32_e32 v15, v15
	v_rndne_f32_e32 v16, v16
	v_rndne_f32_e32 v17, v17
	v_rndne_f32_e32 v10, v10
	v_rndne_f32_e32 v11, v11
	v_rndne_f32_e32 v12, v12
	v_rndne_f32_e32 v13, v13
	v_add_f32_e32 v14, 0x43000000, v14
	v_add_f32_e32 v15, 0x43000000, v15
	v_add_f32_e32 v16, 0x43000000, v16
	v_add_f32_e32 v17, 0x43000000, v17
	v_add_f32_e32 v10, 0x43000000, v10
	v_add_f32_e32 v11, 0x43000000, v11
	v_add_f32_e32 v12, 0x43000000, v12
	v_add_f32_e32 v13, 0x43000000, v13
	v_cvt_pk_u8_f32 v28, v14, 0, 0
	v_cvt_pk_u8_f32 v29, v10, 0, 0
	v_cvt_pk_u8_f32 v28, v15, 1, v28
	v_cvt_pk_u8_f32 v29, v11, 1, v29
	v_cvt_pk_u8_f32 v28, v16, 2, v28
	v_cvt_pk_u8_f32 v29, v12, 2, v29
	v_cvt_pk_u8_f32 v10, v17, 3, v28
	v_cvt_pk_u8_f32 v11, v13, 3, v29
	global_store_dwordx2 v[20:21], v[10:11], off offset:-4
	s_and_saveexec_b64 s[22:23], s[6:7]
	s_cbranch_execz .LBB0_17
	v_ashrrev_i32_e32 v10, 4, v18
	v_ashrrev_i32_e32 v11, 31, v10
	v_mul_f32_e32 v12, 0x41010204, v19
	v_lshl_add_u64 v[10:11], v[10:11], 2, s[12:13]
	global_store_dword v[10:11], v12, off
.LBB0_17:
	s_or_b64 exec, exec, s[22:23]
	s_and_saveexec_b64 s[22:23], s[4:5]
	s_cbranch_execz .LBB0_12
	v_max3_f32 v10, |v2|, 0, |v3|
	v_max3_f32 v10, v10, |v4|, |v5|
	v_max3_f32 v10, v10, |v6|, |v7|
	v_max3_f32 v10, v10, |v8|, |v9|
	v_ashrrev_i32_e32 v23, 31, v22
	s_nop 1
	v_max_f32_dpp v10, v10, v10 quad_perm:[1,0,3,2] row_mask:0xf bank_mask:0xf bound_ctrl:1
	s_nop 1
	v_max_f32_dpp v10, v10, v10 quad_perm:[2,3,0,1] row_mask:0xf bank_mask:0xf bound_ctrl:1
	s_nop 1
	v_max_f32_dpp v10, v10, v10 row_half_mirror row_mask:0xf bank_mask:0xf bound_ctrl:1
	s_nop 1
	v_max_f32_dpp v10, v10, v10 row_mirror row_mask:0xf bank_mask:0xf bound_ctrl:1
	v_div_scale_f32 v11, s[4:5], v10, v10, s26
	v_rcp_f32_e32 v12, v11
	v_div_scale_f32 v13, vcc, s26, v10, s26
	v_fma_f32 v14, -v11, v12, 1.0
	v_fmac_f32_e32 v12, v14, v12
	v_mul_f32_e32 v14, v13, v12
	v_fma_f32 v15, -v11, v14, v13
	v_fmac_f32_e32 v14, v15, v12
	v_fma_f32 v11, -v11, v14, v13
	v_div_fmas_f32 v11, v11, v12, v14
	v_div_fixup_f32 v11, v11, v10, s26
	v_cmp_lt_f32_e32 vcc, 0, v10
	s_nop 1
	v_cndmask_b32_e32 v11, 0, v11, vcc
	v_mul_f32_e32 v2, v2, v11
	v_mul_f32_e32 v3, v3, v11
	v_mul_f32_e32 v4, v4, v11
	v_mul_f32_e32 v5, v5, v11
	v_mul_f32_e32 v6, v6, v11
	v_mul_f32_e32 v7, v7, v11
	v_mul_f32_e32 v8, v8, v11
	v_mul_f32_e32 v9, v9, v11
	v_rndne_f32_e32 v2, v2
	v_rndne_f32_e32 v3, v3
	v_rndne_f32_e32 v4, v4
	v_rndne_f32_e32 v5, v5
	v_rndne_f32_e32 v6, v6
	v_rndne_f32_e32 v7, v7
	v_rndne_f32_e32 v8, v8
	v_rndne_f32_e32 v9, v9
	v_add_f32_e32 v2, 0x43000000, v2
	v_add_f32_e32 v3, 0x43000000, v3
	v_add_f32_e32 v4, 0x43000000, v4
	v_add_f32_e32 v5, 0x43000000, v5
	v_add_f32_e32 v6, 0x43000000, v6
	v_add_f32_e32 v7, 0x43000000, v7
	v_add_f32_e32 v8, 0x43000000, v8
	v_add_f32_e32 v9, 0x43000000, v9
	v_cvt_pk_u8_f32 v12, v2, 0, 0
	v_cvt_pk_u8_f32 v13, v6, 0, 0
	v_cvt_pk_u8_f32 v12, v3, 1, v12
	v_cvt_pk_u8_f32 v13, v7, 1, v13
	v_cvt_pk_u8_f32 v12, v4, 2, v12
	v_cvt_pk_u8_f32 v13, v8, 2, v13
	v_cvt_pk_u8_f32 v2, v5, 3, v12
	v_cvt_pk_u8_f32 v3, v9, 3, v13
	v_lshl_add_u64 v[4:5], v[22:23], 3, s[8:9]
	global_store_dwordx2 v[4:5], v[2:3], off
	s_and_b64 exec, exec, s[6:7]
	s_cbranch_execz .LBB0_12
	v_ashrrev_i32_e32 v2, 4, v22
	v_ashrrev_i32_e32 v3, 31, v2
	v_mul_f32_e32 v4, 0x41010204, v10
	v_lshl_add_u64 v[2:3], v[2:3], 2, s[12:13]
	global_store_dword v[2:3], v4, off
	s_branch .LBB0_12
